# v62 plus P0 cos/sin table loop: the eight position loads of a thread prefetched before the loop (fast path when the grid stride gives exactly 8 iterations; generic loop kept)
# speedup vs baseline: 1.0143x; 1.0024x over previous
.LBB0_45:
	s_mov_b32 s2, 0x100000
	v_cmp_gt_i32_e32 vcc, s2, v80
	s_and_saveexec_b64 s[2:3], vcc
	s_cbranch_execz .LBB0_48
	v_ashrrev_i32_e32 v81, 31, v80
	v_lshl_add_u64 v[2:3], v[80:81], 2, s[0:1]
	s_mov_b64 s[0:1], 0xeb00000
	s_ashr_i32 s7, s6, 31
	v_lshlrev_b32_e32 v1, 1, v1
	v_lshl_add_u64 v[2:3], v[2:3], 0, s[0:1]
	s_lshl_b64 s[0:1], s[6:7], 2
	v_lshl_add_u32 v1, s80, 10, v1
	s_lshl_b32 s7, s81, 10
	s_mov_b64 s[8:9], 0
	s_mov_b32 s10, 0xc2fc0000
	v_mov_b32_e32 v4, 0x42800000
	v_not_b32_e32 v5, 63
	s_mov_b32 s11, 0xfffff
	s_cmp_lg_u32 s6, 0x20000
	s_cbranch_scc1 .LBB0_47
	s_mov_b32 s98, 0x1000
	s_mov_b32 s99, 0
	v_ashrrev_i32_e32 v6, 7, v80
	v_ashrrev_i32_e32 v7, 31, v6
	v_lshl_add_u64 v[6:7], v[6:7], 2, s[12:13]
	global_load_dword v20, v[6:7], off
	v_lshl_add_u64 v[6:7], v[6:7], 0, s[98:99]
	global_load_dword v21, v[6:7], off
	v_lshl_add_u64 v[6:7], v[6:7], 0, s[98:99]
	global_load_dword v22, v[6:7], off
	v_lshl_add_u64 v[6:7], v[6:7], 0, s[98:99]
	global_load_dword v23, v[6:7], off
	v_lshl_add_u64 v[6:7], v[6:7], 0, s[98:99]
	global_load_dword v24, v[6:7], off
	v_lshl_add_u64 v[6:7], v[6:7], 0, s[98:99]
	global_load_dword v25, v[6:7], off
	v_lshl_add_u64 v[6:7], v[6:7], 0, s[98:99]
	global_load_dword v26, v[6:7], off
	v_lshl_add_u64 v[6:7], v[6:7], 0, s[98:99]
	global_load_dword v27, v[6:7], off
	s_waitcnt vmcnt(0)
.Lcs_fast:
	v_mov_b32_e32 v8, v20
	v_mov_b32_e32 v20, v21
	v_mov_b32_e32 v21, v22
	v_mov_b32_e32 v22, v23
	v_mov_b32_e32 v23, v24
	v_mov_b32_e32 v24, v25
	v_mov_b32_e32 v25, v26
	v_mov_b32_e32 v26, v27
	v_and_b32_e32 v7, 0xfe, v1
	v_cvt_f32_ubyte0_e32 v9, v7
	v_mul_f32_e32 v10, 0xbd549a78, v9
	v_cmp_gt_f32_e64 s[4:5], s10, v10
	v_add_co_u32_e32 v6, vcc, 0x400000, v2
	s_nop 0
	v_cndmask_b32_e64 v10, 0, v4, s[4:5]
	v_fmac_f32_e32 v10, 0xbd549a78, v9
	v_exp_f32_e32 v10, v10
	v_cndmask_b32_e64 v9, 0, v5, s[4:5]
	v_add_u32_e32 v80, s6, v80
	v_addc_co_u32_e32 v7, vcc, 0, v3, vcc
	v_ldexp_f32 v9, v10, v9
	v_cmp_lt_i32_e32 vcc, s11, v80
	v_add_u32_e32 v1, s7, v1
	s_or_b64 s[8:9], vcc, s[8:9]
	v_cvt_f32_i32_e32 v8, v8
	v_mul_f32_e32 v8, v9, v8
	v_mul_f32_e32 v9, 0.15915494, v8
	v_floor_f32_e32 v9, v9
	v_fma_f32 v8, v8, 0.15915494, -v9
	v_cos_f32_e32 v9, v8
	v_sin_f32_e32 v8, v8
	global_store_dword v[2:3], v9, off
	global_store_dword v[6:7], v8, off
	v_lshl_add_u64 v[2:3], v[2:3], 0, s[0:1]
	s_andn2_b64 exec, exec, s[8:9]
	s_cbranch_execnz .Lcs_fast
	s_branch .LBB0_48
